# baseline (speedup 1.0000x reference)
.LBB2_9:
	v_mad_i64_i32 v[0:1], s[12:13], v110, 48, 0
	v_or_b32_e32 v0, v0, v108
	v_lshlrev_b64 v[0:1], 8, v[0:1]
	v_lshl_add_u64 v[0:1], v[114:115], 0, v[0:1]
	v_add_co_u32_e32 v2, vcc, s15, v0
	global_load_dwordx4 v[24:27], v[0:1], off nt
	s_nop 0
	v_addc_co_u32_e32 v3, vcc, 0, v1, vcc
	v_add_co_u32_e32 v126, vcc, 0x2000, v0
	v_ashrrev_i32_e32 v111, 31, v110
	s_nop 0
	v_addc_co_u32_e32 v127, vcc, 0, v1, vcc
	global_load_dwordx4 v[64:67], v[2:3], off nt
	global_load_dwordx4 v[68:71], v[126:127], off nt
	global_load_dwordx4 v[20:23], v[0:1], off offset:64 nt
	global_load_dwordx4 v[56:59], v[2:3], off offset:64 nt
	global_load_dwordx4 v[60:63], v[126:127], off offset:64 nt
	global_load_dwordx4 v[40:43], v[2:3], off offset:128 nt
	global_load_dwordx4 v[16:19], v[0:1], off offset:128 nt
	global_load_dwordx4 v[44:47], v[126:127], off offset:128 nt
	global_load_dwordx4 v[28:31], v[2:3], off offset:192 nt
	global_load_dwordx4 v[12:15], v[0:1], off offset:192 nt
	global_load_dwordx4 v[32:35], v[126:127], off offset:192 nt
	s_mov_b32 s12, 11
	v_mov_b32_e32 v72, v116
	s_mov_b32 s13, 0
	v_mov_b32_e32 v73, v109
	v_add_u32_e32 v121, v109, v112
	v_add_u32_e32 v122, 0x1f200, v112
	v_add_u32_e32 v124, v116, v112
	v_add_u32_e32 v124, 0x17600, v124
	v_mov_b32_e32 v0, 0
	v_mov_b32_e32 v1, v113
	v_mov_b32_e32 v2, v113
	v_mov_b32_e32 v3, v113
	v_mov_b32_e32 v36, 0
	v_mov_b32_e32 v37, v113
	v_mov_b32_e32 v38, v113
	v_mov_b32_e32 v39, v113
	v_mov_b32_e32 v48, 0
	v_mov_b32_e32 v49, v113
	v_mov_b32_e32 v50, v113
	v_mov_b32_e32 v51, v113
	v_mov_b32_e32 v52, 0
	v_mov_b32_e32 v53, v113
	v_mov_b32_e32 v54, v113
	v_mov_b32_e32 v55, v113
	v_mov_b32_e32 v4, 0
	v_mov_b32_e32 v5, v113
	v_mov_b32_e32 v6, v113
	v_mov_b32_e32 v7, v113
	v_mov_b32_e32 v8, 0
	v_mov_b32_e32 v9, v113
	v_mov_b32_e32 v10, v113
	v_mov_b32_e32 v11, v113
.LBB2_10:
	s_setprio 0
	ds_read_b128 v[74:77], v121
	ds_read_b128 v[78:81], v122
	ds_read_b128 v[82:85], v121 offset:64
	s_waitcnt vmcnt(11) lgkmcnt(0)
	v_mfma_f32_16x16x32_bf16 v[86:89], v[74:77], v[24:27], v[78:81]
	s_waitcnt vmcnt(10)
	v_mfma_f32_16x16x32_bf16 v[90:93], v[74:77], v[64:67], v[78:81]
	s_waitcnt vmcnt(9)
	v_mfma_f32_16x16x32_bf16 v[74:77], v[74:77], v[68:71], v[78:81]
	s_waitcnt vmcnt(7)
	v_mfma_f32_16x16x32_bf16 v[78:81], v[82:85], v[20:23], v[86:89]
	v_mfma_f32_16x16x32_bf16 v[86:89], v[82:85], v[56:59], v[90:93]
	s_waitcnt vmcnt(6)
	v_mfma_f32_16x16x32_bf16 v[74:77], v[82:85], v[60:63], v[74:77]
	ds_read_b128 v[82:85], v121 offset:128
	s_nop 0
	ds_read_b128 v[90:93], v121 offset:192
	s_waitcnt vmcnt(4) lgkmcnt(1)
	v_mfma_f32_16x16x32_bf16 v[86:89], v[82:85], v[40:43], v[86:89]
	v_mfma_f32_16x16x32_bf16 v[78:81], v[82:85], v[16:19], v[78:81]
	s_waitcnt vmcnt(3)
	v_mfma_f32_16x16x32_bf16 v[74:77], v[82:85], v[44:47], v[74:77]
	s_waitcnt vmcnt(1) lgkmcnt(0)
	v_mfma_f32_16x16x32_bf16 v[82:85], v[90:93], v[28:31], v[86:89]
	s_nop 2
	ds_read_b128 v[86:89], v121 offset:4352
	v_mfma_f32_16x16x32_bf16 v[78:81], v[90:93], v[12:15], v[78:81]
	s_waitcnt vmcnt(0)
	v_mfma_f32_16x16x32_bf16 v[74:77], v[90:93], v[32:35], v[74:77]
	ds_read_b128 v[90:93], v122 offset:64
	ds_read_b128 v[94:97], v121 offset:4416
	s_waitcnt lgkmcnt(1)
	v_mfma_f32_16x16x32_bf16 v[98:101], v[86:89], v[24:27], v[90:93]
	v_mfma_f32_16x16x32_bf16 v[102:105], v[86:89], v[64:67], v[90:93]
	v_mfma_f32_16x16x32_bf16 v[86:89], v[86:89], v[68:71], v[90:93]
	s_waitcnt lgkmcnt(0)
	v_mfma_f32_16x16x32_bf16 v[90:93], v[94:97], v[20:23], v[98:101]
	v_mfma_f32_16x16x32_bf16 v[98:101], v[94:97], v[56:59], v[102:105]
	v_mfma_f32_16x16x32_bf16 v[86:89], v[94:97], v[60:63], v[86:89]
	ds_read_b128 v[94:97], v121 offset:4480
	s_nop 1
	ds_read_b128 v[102:105], v121 offset:4544
	s_waitcnt lgkmcnt(1)
	v_mfma_f32_16x16x32_bf16 v[90:93], v[94:97], v[16:19], v[90:93]
	v_mfma_f32_16x16x32_bf16 v[98:101], v[94:97], v[40:43], v[98:101]
	v_mfma_f32_16x16x32_bf16 v[86:89], v[94:97], v[44:47], v[86:89]
	s_waitcnt lgkmcnt(0)
	v_mfma_f32_16x16x32_bf16 v[90:93], v[102:105], v[12:15], v[90:93]
	v_mfma_f32_16x16x32_bf16 v[94:97], v[102:105], v[28:31], v[98:101]
	v_mfma_f32_16x16x32_bf16 v[86:89], v[102:105], v[32:35], v[86:89]
	s_setprio 2
	s_nop 1
	v_exp_f32_e32 v99, v78
	v_exp_f32_e32 v100, v79
	v_exp_f32_e32 v101, v80
	v_exp_f32_e32 v102, v81
	v_exp_f32_e32 v90, v90
	v_exp_f32_e32 v91, v91
	v_exp_f32_e32 v92, v92
	v_exp_f32_e32 v93, v93
	v_exp_f32_e32 v103, v74
	v_exp_f32_e32 v104, v75
	v_exp_f32_e32 v105, v76
	v_exp_f32_e32 v106, v77
	v_exp_f32_e32 v88, v88
	v_exp_f32_e32 v89, v89
	v_exp_f32_e32 v82, v82
	v_exp_f32_e32 v83, v83
	v_exp_f32_e32 v84, v84
	v_exp_f32_e32 v85, v85
	v_add_f32_e32 v98, 1.0, v99
	v_add_f32_e32 v99, 1.0, v100
	v_add_f32_e32 v100, 1.0, v101
	v_add_f32_e32 v101, 1.0, v102
	v_add_f32_e32 v90, 1.0, v90
	v_add_f32_e32 v91, 1.0, v91
	v_add_f32_e32 v92, 1.0, v92
	v_add_f32_e32 v93, 1.0, v93
	v_exp_f32_e32 v94, v94
	v_exp_f32_e32 v95, v95
	v_exp_f32_e32 v96, v96
	v_exp_f32_e32 v97, v97
	v_exp_f32_e32 v86, v86
	v_exp_f32_e32 v87, v87
	ds_read_b128 v[74:77], v124
	ds_read_b128 v[78:81], v124 offset:11520
	v_add_f32_e32 v102, 1.0, v103
	v_add_f32_e32 v103, 1.0, v104
	v_add_f32_e32 v104, 1.0, v105
	v_add_f32_e32 v105, 1.0, v106
	v_add_f32_e32 v106, 1.0, v88
	v_add_f32_e32 v107, 1.0, v89
	v_rcp_f32_e32 v88, v98
	v_rcp_f32_e32 v89, v99
	v_rcp_f32_e32 v98, v100
	v_rcp_f32_e32 v99, v101
	v_rcp_f32_e32 v90, v90
	v_rcp_f32_e32 v91, v91
	v_rcp_f32_e32 v92, v92
	v_rcp_f32_e32 v93, v93
	v_add_f32_e32 v82, 1.0, v82
	v_add_f32_e32 v83, 1.0, v83
	v_add_f32_e32 v84, 1.0, v84
	v_add_f32_e32 v85, 1.0, v85
	v_add_f32_e32 v94, 1.0, v94
	v_add_f32_e32 v95, 1.0, v95
	v_add_f32_e32 v96, 1.0, v96
	v_add_f32_e32 v97, 1.0, v97
	v_add_f32_e32 v86, 1.0, v86
	v_add_f32_e32 v87, 1.0, v87
	v_rcp_f32_e32 v100, v82
	v_rcp_f32_e32 v101, v83
	v_rcp_f32_e32 v119, v84
	v_rcp_f32_e32 v120, v85
	v_cvt_pk_bf16_f32 v82, v88, v89
	v_cvt_pk_bf16_f32 v83, v98, v99
	v_cvt_pk_bf16_f32 v84, v90, v91
	v_cvt_pk_bf16_f32 v85, v92, v93
	v_rcp_f32_e32 v94, v94
	v_rcp_f32_e32 v95, v95
	v_rcp_f32_e32 v96, v96
	v_rcp_f32_e32 v97, v97
	v_rcp_f32_e32 v102, v102
	v_rcp_f32_e32 v103, v103
	v_rcp_f32_e32 v104, v104
	v_rcp_f32_e32 v105, v105
	s_waitcnt lgkmcnt(1)
	v_mfma_f32_16x16x32_bf16 v[52:55], v[74:77], v[82:85], v[52:55]
	v_rcp_f32_e32 v90, v86
	v_rcp_f32_e32 v91, v87
	v_rcp_f32_e32 v92, v107
	s_waitcnt lgkmcnt(0)
	v_mfma_f32_16x16x32_bf16 v[0:3], v[78:81], v[82:85], v[0:3]
	v_rcp_f32_e32 v85, v106
	v_cvt_pk_bf16_f32 v86, v100, v101
	v_cvt_pk_bf16_f32 v87, v119, v120
	v_cvt_pk_bf16_f32 v88, v94, v95
	v_cvt_pk_bf16_f32 v89, v96, v97
	v_cvt_pk_bf16_f32 v82, v102, v103
	v_cvt_pk_bf16_f32 v83, v104, v105
	v_cvt_pk_bf16_f32 v84, v90, v91
	v_cvt_pk_bf16_f32 v85, v85, v92
	v_mfma_f32_16x16x32_bf16 v[48:51], v[74:77], v[86:89], v[48:51]
	s_add_i32 s12, s12, -1
	v_add_u32_e32 v121, 0x2200, v121
	v_add_u32_e32 v122, 0x80, v122
	v_mfma_f32_16x16x32_bf16 v[4:7], v[78:81], v[86:89], v[4:7]
	s_cmp_eq_u32 s12, 0
	v_add_u32_e32 v124, 64, v124
	v_mfma_f32_16x16x32_bf16 v[36:39], v[74:77], v[82:85], v[36:39]
	v_mfma_f32_16x16x32_bf16 v[8:11], v[78:81], v[82:85], v[8:11]
	s_cbranch_scc0 .LBB2_10
	ds_read_b128 v[72:75], v117
	ds_read_b128 v[76:79], v117 offset:64
	s_waitcnt lgkmcnt(1)
	v_mfma_f32_16x16x32_bf16 v[80:83], v[72:75], v[24:27], 0
	v_mfma_f32_16x16x32_bf16 v[84:87], v[72:75], v[64:67], 0
	v_mfma_f32_16x16x32_bf16 v[72:75], v[72:75], v[68:71], 0
	s_waitcnt lgkmcnt(0)
	v_mfma_f32_16x16x32_bf16 v[88:91], v[76:79], v[20:23], v[80:83]
	s_nop 3
	ds_read_b128 v[80:83], v117 offset:128
	ds_read_b128 v[96:99], v117 offset:192
	v_mfma_f32_16x16x32_bf16 v[84:87], v[76:79], v[56:59], v[84:87]
	v_mfma_f32_16x16x32_bf16 v[100:103], v[76:79], v[60:63], v[72:75]
	s_nop 2
	v_add_u32_e32 v72, 0, v112
	v_add_u32_e32 v92, 0x1f780, v72
	ds_read_b128 v[72:75], v92
	s_waitcnt lgkmcnt(2)
	v_mfma_f32_16x16x32_bf16 v[84:87], v[80:83], v[40:43], v[84:87]
	s_waitcnt lgkmcnt(0)
	v_add_f32_e32 v52, v72, v52
	v_mfma_f32_16x16x32_bf16 v[104:107], v[80:83], v[16:19], v[88:91]
	v_add_f32_e32 v48, v72, v48
	v_exp_f32_e32 v52, v52
	v_exp_f32_e32 v48, v48
	v_mfma_f32_16x16x32_bf16 v[80:83], v[80:83], v[44:47], v[100:103]
	v_add_f32_e32 v36, v72, v36
	v_exp_f32_e32 v36, v36
	v_add_f32_e32 v72, v52, v48
	v_mfma_f32_16x16x32_bf16 v[84:87], v[96:99], v[28:31], v[84:87]
	ds_read_b128 v[88:91], v117 offset:4352
	ds_read_b128 v[76:79], v117 offset:4416
	ds_read_b128 v[92:95], v92 offset:64
	v_add_f32_e32 v72, v72, v36
	v_add_f32_e32 v49, v73, v49
	v_mfma_f32_16x16x32_bf16 v[100:103], v[96:99], v[12:15], v[104:107]
	s_nop 1
	v_mul_f32_e32 v48, v48, v84
	v_exp_f32_e32 v49, v49
	v_add_f32_e32 v37, v73, v37
	v_mfma_f32_16x16x32_bf16 v[80:83], v[96:99], v[32:35], v[80:83]
	v_exp_f32_e32 v37, v37
	s_nop 0
	v_fmac_f32_e32 v48, v52, v100
	v_add_f32_e32 v52, v73, v53
	v_exp_f32_e32 v52, v52
	s_waitcnt lgkmcnt(2)
	v_mfma_f32_16x16x32_bf16 v[24:27], v[88:91], v[24:27], 0
	s_nop 0
	v_fmac_f32_e32 v48, v36, v80
	v_add_f32_dpp v36, v72, v72 quad_perm:[1,0,3,2] row_mask:0xf bank_mask:0xf bound_ctrl:1
	ds_read_b128 v[104:107], v117 offset:4480
	ds_read_b128 v[120:123], v117 offset:4544
	v_add_f32_dpp v36, v36, v36 quad_perm:[2,3,0,1] row_mask:0xf bank_mask:0xf bound_ctrl:1
	v_add_f32_dpp v48, v48, v48 quad_perm:[1,0,3,2] row_mask:0xf bank_mask:0xf bound_ctrl:1
	v_mfma_f32_16x16x32_bf16 v[64:67], v[88:91], v[64:67], 0
	v_add_f32_dpp v36, v36, v36 row_half_mirror row_mask:0xf bank_mask:0xf bound_ctrl:1
	v_add_f32_dpp v48, v48, v48 quad_perm:[2,3,0,1] row_mask:0xf bank_mask:0xf bound_ctrl:1
	v_add_f32_e32 v50, v74, v50
	v_add_f32_dpp v36, v36, v36 row_mirror row_mask:0xf bank_mask:0xf bound_ctrl:1
	v_rcp_f32_e32 v36, v36
	v_add_f32_dpp v48, v48, v48 row_half_mirror row_mask:0xf bank_mask:0xf bound_ctrl:1
	s_waitcnt lgkmcnt(3)
	v_mfma_f32_16x16x32_bf16 v[20:23], v[76:79], v[20:23], v[24:27]
	v_exp_f32_e32 v50, v50
	v_add_f32_dpp v48, v48, v48 row_mirror row_mask:0xf bank_mask:0xf bound_ctrl:1
	v_fma_f32 v36, v36, v48, 0
	v_add_f32_e32 v48, v52, v49
	v_mul_f32_e32 v49, v49, v85
	v_add_f32_e32 v48, v48, v37
	v_fmac_f32_e32 v49, v52, v101
	v_fmac_f32_e32 v49, v37, v81
	v_mfma_f32_16x16x32_bf16 v[68:71], v[88:91], v[68:71], 0
	v_add_f32_dpp v37, v48, v48 quad_perm:[1,0,3,2] row_mask:0xf bank_mask:0xf bound_ctrl:1
	v_add_f32_dpp v24, v49, v49 quad_perm:[1,0,3,2] row_mask:0xf bank_mask:0xf bound_ctrl:1
	v_add_f32_e32 v49, v74, v54
	v_add_f32_dpp v37, v37, v37 quad_perm:[2,3,0,1] row_mask:0xf bank_mask:0xf bound_ctrl:1
	v_add_f32_dpp v48, v24, v24 quad_perm:[2,3,0,1] row_mask:0xf bank_mask:0xf bound_ctrl:1
	v_mfma_f32_16x16x32_bf16 v[24:27], v[76:79], v[56:59], v[64:67]
	v_add_f32_dpp v37, v37, v37 row_half_mirror row_mask:0xf bank_mask:0xf bound_ctrl:1
	v_exp_f32_e32 v49, v49
	v_add_f32_dpp v48, v48, v48 row_half_mirror row_mask:0xf bank_mask:0xf bound_ctrl:1
	v_add_f32_dpp v37, v37, v37 row_mirror row_mask:0xf bank_mask:0xf bound_ctrl:1
	s_waitcnt lgkmcnt(1)
	v_mfma_f32_16x16x32_bf16 v[16:19], v[104:107], v[16:19], v[20:23]
	v_rcp_f32_e32 v37, v37
	v_add_f32_dpp v48, v48, v48 row_mirror row_mask:0xf bank_mask:0xf bound_ctrl:1
	v_add_f32_e32 v0, v92, v0
	v_add_f32_e32 v20, v74, v38
	v_mfma_f32_16x16x32_bf16 v[56:59], v[76:79], v[60:63], v[68:71]
	v_exp_f32_e32 v38, v20
	v_fmac_f32_e32 v36, v37, v48
	v_add_f32_e32 v4, v92, v4
	v_mfma_f32_16x16x32_bf16 v[20:23], v[104:107], v[40:43], v[24:27]
	v_mul_f32_e32 v40, v50, v86
	v_fmac_f32_e32 v40, v49, v102
	v_fmac_f32_e32 v40, v38, v82
	v_add_f32_e32 v24, v49, v50
	v_add_f32_e32 v37, v24, v38
	v_mfma_f32_16x16x32_bf16 v[24:27], v[104:107], v[44:47], v[56:59]
	v_exp_f32_e32 v0, v0
	v_exp_f32_e32 v4, v4
	v_add_f32_e32 v8, v92, v8
	s_waitcnt lgkmcnt(0)
	v_mfma_f32_16x16x32_bf16 v[12:15], v[120:123], v[12:15], v[16:19]
	v_exp_f32_e32 v8, v8
	v_add_f32_e32 v1, v93, v1
	v_add_f32_e32 v5, v93, v5
	v_add_f32_dpp v16, v37, v37 quad_perm:[1,0,3,2] row_mask:0xf bank_mask:0xf bound_ctrl:1
	v_exp_f32_e32 v1, v1
	v_exp_f32_e32 v5, v5
	v_add_f32_dpp v16, v16, v16 quad_perm:[2,3,0,1] row_mask:0xf bank_mask:0xf bound_ctrl:1
	v_add_f32_e32 v2, v94, v2
	v_exp_f32_e32 v2, v2
	v_add_f32_dpp v37, v16, v16 row_half_mirror row_mask:0xf bank_mask:0xf bound_ctrl:1
	v_mfma_f32_16x16x32_bf16 v[16:19], v[120:123], v[28:31], v[20:23]
	s_nop 0
	v_add_f32_dpp v28, v37, v37 row_mirror row_mask:0xf bank_mask:0xf bound_ctrl:1
	s_nop 0
	v_add_f32_dpp v20, v40, v40 quad_perm:[1,0,3,2] row_mask:0xf bank_mask:0xf bound_ctrl:1
	s_nop 1
	v_add_f32_dpp v29, v20, v20 quad_perm:[2,3,0,1] row_mask:0xf bank_mask:0xf bound_ctrl:1
	v_mfma_f32_16x16x32_bf16 v[20:23], v[120:123], v[32:35], v[24:27]
	s_nop 2
	v_add_f32_e32 v26, v75, v55
	v_add_f32_e32 v27, v75, v51
	v_rcp_f32_e32 v25, v28
	v_exp_f32_e32 v26, v26
	v_exp_f32_e32 v27, v27
	v_add_f32_e32 v28, v75, v39
	v_exp_f32_e32 v28, v28
	v_add_f32_dpp v24, v29, v29 row_half_mirror row_mask:0xf bank_mask:0xf bound_ctrl:1
	s_nop 1
	v_add_f32_dpp v24, v24, v24 row_mirror row_mask:0xf bank_mask:0xf bound_ctrl:1
	v_fmac_f32_e32 v36, v25, v24
	v_add_f32_e32 v24, v26, v27
	v_add_f32_e32 v24, v24, v28
	v_mul_f32_e32 v25, v27, v87
	v_fmac_f32_e32 v25, v26, v103
	v_add_f32_dpp v24, v24, v24 quad_perm:[1,0,3,2] row_mask:0xf bank_mask:0xf bound_ctrl:1
	v_fmac_f32_e32 v25, v28, v83
	s_nop 0
	v_add_f32_dpp v24, v24, v24 quad_perm:[2,3,0,1] row_mask:0xf bank_mask:0xf bound_ctrl:1
	v_add_f32_dpp v25, v25, v25 quad_perm:[1,0,3,2] row_mask:0xf bank_mask:0xf bound_ctrl:1
	s_nop 0
	v_add_f32_dpp v24, v24, v24 row_half_mirror row_mask:0xf bank_mask:0xf bound_ctrl:1
	v_add_f32_dpp v25, v25, v25 quad_perm:[2,3,0,1] row_mask:0xf bank_mask:0xf bound_ctrl:1
	s_nop 0
	v_add_f32_dpp v24, v24, v24 row_mirror row_mask:0xf bank_mask:0xf bound_ctrl:1
	v_rcp_f32_e32 v24, v24
	v_add_f32_dpp v25, v25, v25 row_half_mirror row_mask:0xf bank_mask:0xf bound_ctrl:1
	s_nop 1
	v_add_f32_dpp v25, v25, v25 row_mirror row_mask:0xf bank_mask:0xf bound_ctrl:1
	v_fmac_f32_e32 v36, v24, v25
	v_add_f32_e32 v24, v0, v4
	v_add_f32_e32 v24, v24, v8
	v_mul_f32_e32 v4, v4, v16
	v_fmac_f32_e32 v4, v0, v12
	v_add_f32_dpp v0, v24, v24 quad_perm:[1,0,3,2] row_mask:0xf bank_mask:0xf bound_ctrl:1
	v_fmac_f32_e32 v4, v8, v20
	v_add_f32_e32 v8, v93, v9
	v_add_f32_dpp v0, v0, v0 quad_perm:[2,3,0,1] row_mask:0xf bank_mask:0xf bound_ctrl:1
	v_add_f32_dpp v4, v4, v4 quad_perm:[1,0,3,2] row_mask:0xf bank_mask:0xf bound_ctrl:1
	v_exp_f32_e32 v8, v8
	v_add_f32_dpp v0, v0, v0 row_half_mirror row_mask:0xf bank_mask:0xf bound_ctrl:1
	v_add_f32_dpp v4, v4, v4 quad_perm:[2,3,0,1] row_mask:0xf bank_mask:0xf bound_ctrl:1
	s_nop 0
	v_add_f32_dpp v0, v0, v0 row_mirror row_mask:0xf bank_mask:0xf bound_ctrl:1
	v_rcp_f32_e32 v0, v0
	v_add_f32_dpp v4, v4, v4 row_half_mirror row_mask:0xf bank_mask:0xf bound_ctrl:1
	s_nop 1
	v_add_f32_dpp v4, v4, v4 row_mirror row_mask:0xf bank_mask:0xf bound_ctrl:1
	v_fmac_f32_e32 v36, v0, v4
	v_add_f32_e32 v0, v1, v5
	v_add_f32_e32 v0, v0, v8
	v_mul_f32_e32 v4, v5, v17
	v_fmac_f32_e32 v4, v1, v13
	v_add_f32_dpp v0, v0, v0 quad_perm:[1,0,3,2] row_mask:0xf bank_mask:0xf bound_ctrl:1
	v_fmac_f32_e32 v4, v8, v21
	v_add_f32_e32 v5, v94, v10
	v_add_f32_dpp v0, v0, v0 quad_perm:[2,3,0,1] row_mask:0xf bank_mask:0xf bound_ctrl:1
	v_add_f32_dpp v1, v4, v4 quad_perm:[1,0,3,2] row_mask:0xf bank_mask:0xf bound_ctrl:1
	v_add_f32_e32 v4, v94, v6
	v_add_f32_dpp v0, v0, v0 row_half_mirror row_mask:0xf bank_mask:0xf bound_ctrl:1
	v_exp_f32_e32 v4, v4
	v_add_f32_dpp v1, v1, v1 quad_perm:[2,3,0,1] row_mask:0xf bank_mask:0xf bound_ctrl:1
	v_add_f32_dpp v0, v0, v0 row_mirror row_mask:0xf bank_mask:0xf bound_ctrl:1
	v_rcp_f32_e32 v0, v0
	v_exp_f32_e32 v5, v5
	v_add_f32_dpp v1, v1, v1 row_half_mirror row_mask:0xf bank_mask:0xf bound_ctrl:1
	s_nop 1
	v_add_f32_dpp v1, v1, v1 row_mirror row_mask:0xf bank_mask:0xf bound_ctrl:1
	v_fmac_f32_e32 v36, v0, v1
	v_add_f32_e32 v0, v2, v4
	v_add_f32_e32 v0, v0, v5
	v_mul_f32_e32 v1, v4, v18
	v_fmac_f32_e32 v1, v2, v14
	v_add_f32_dpp v0, v0, v0 quad_perm:[1,0,3,2] row_mask:0xf bank_mask:0xf bound_ctrl:1
	v_fmac_f32_e32 v1, v5, v22
	v_add_f32_e32 v2, v95, v3
	v_add_f32_dpp v0, v0, v0 quad_perm:[2,3,0,1] row_mask:0xf bank_mask:0xf bound_ctrl:1
	v_add_f32_e32 v3, v95, v7
	v_add_f32_dpp v1, v1, v1 quad_perm:[1,0,3,2] row_mask:0xf bank_mask:0xf bound_ctrl:1
	v_add_f32_dpp v0, v0, v0 row_half_mirror row_mask:0xf bank_mask:0xf bound_ctrl:1
	v_exp_f32_e32 v2, v2
	v_exp_f32_e32 v3, v3
	v_add_f32_dpp v0, v0, v0 row_mirror row_mask:0xf bank_mask:0xf bound_ctrl:1
	v_rcp_f32_e32 v0, v0
	v_add_f32_e32 v4, v95, v11
	v_add_f32_dpp v1, v1, v1 quad_perm:[2,3,0,1] row_mask:0xf bank_mask:0xf bound_ctrl:1
	v_exp_f32_e32 v4, v4
	s_nop 0
	v_add_f32_dpp v1, v1, v1 row_half_mirror row_mask:0xf bank_mask:0xf bound_ctrl:1
	s_nop 1
	v_add_f32_dpp v1, v1, v1 row_mirror row_mask:0xf bank_mask:0xf bound_ctrl:1
	v_fmac_f32_e32 v36, v0, v1
	v_add_f32_e32 v0, v2, v3
	v_add_f32_e32 v0, v0, v4
	v_mul_f32_e32 v1, v3, v19
	v_fmac_f32_e32 v1, v2, v15
	v_add_f32_dpp v0, v0, v0 quad_perm:[1,0,3,2] row_mask:0xf bank_mask:0xf bound_ctrl:1
	v_fmac_f32_e32 v1, v4, v23
	s_nop 0
	v_add_f32_dpp v0, v0, v0 quad_perm:[2,3,0,1] row_mask:0xf bank_mask:0xf bound_ctrl:1
	v_add_f32_dpp v1, v1, v1 quad_perm:[1,0,3,2] row_mask:0xf bank_mask:0xf bound_ctrl:1
	s_nop 0
	v_add_f32_dpp v0, v0, v0 row_half_mirror row_mask:0xf bank_mask:0xf bound_ctrl:1
	v_add_f32_dpp v1, v1, v1 quad_perm:[2,3,0,1] row_mask:0xf bank_mask:0xf bound_ctrl:1
	s_nop 0
	v_add_f32_dpp v0, v0, v0 row_mirror row_mask:0xf bank_mask:0xf bound_ctrl:1
	v_rcp_f32_e32 v0, v0
	v_add_f32_dpp v1, v1, v1 row_half_mirror row_mask:0xf bank_mask:0xf bound_ctrl:1
	s_nop 1
	v_add_f32_dpp v1, v1, v1 row_mirror row_mask:0xf bank_mask:0xf bound_ctrl:1
	v_fmac_f32_e32 v36, v0, v1
	s_nop 0
	v_readlane_b32 s20, v36, 0
	v_readlane_b32 s23, v36, 16
	v_readlane_b32 s21, v36, 32
	v_readlane_b32 s22, v36, 48
	s_and_saveexec_b64 s[12:13], s[0:1]
	s_cbranch_execz .LBB2_8
	v_lshlrev_b64 v[0:1], 2, v[110:111]
	v_lshl_add_u64 v[2:3], s[4:5], 0, v[0:1]
	global_load_dword v4, v[2:3], off
	v_lshl_add_u64 v[2:3], s[6:7], 0, v[0:1]
	global_load_dword v5, v[2:3], off
	v_mov_b32_e32 v2, s23
	v_add_f32_e32 v2, s20, v2
	v_add_f32_e32 v2, s21, v2
	v_add_f32_e32 v2, s22, v2
	v_add_f32_e32 v6, s14, v2
	v_max_f32_e64 v7, -v6, 0
	v_mul_f32_e32 v2, 0xbfb8aa3b, v6
	v_sub_f32_e64 v8, -v6, v7
	v_exp_f32_e32 v2, v2
	v_mul_f32_e32 v3, 0xbfb8aa3b, v7
	v_mul_f32_e32 v8, 0x3fb8aa3b, v8
	v_exp_f32_e32 v3, v3
	v_exp_f32_e32 v8, v8
	v_add_f32_e32 v2, 1.0, v2
	v_rcp_f32_e32 v9, v2
	v_add_f32_e32 v2, v3, v8
	v_cmp_gt_f32_e32 vcc, s17, v2
	s_and_b64 s[20:21], vcc, exec
	s_cselect_b32 s20, 32, 0
	v_ldexp_f32 v2, v2, s20
	v_log_f32_e32 v10, v2
	v_lshl_add_u64 v[2:3], s[8:9], 0, v[0:1]
	global_store_dword v[2:3], v9, off
	v_cndmask_b32_e32 v8, 0, v118, vcc
	v_mul_f32_e32 v2, 0x3f317217, v10
	v_fma_f32 v2, v10, s18, -v2
	v_fmac_f32_e32 v2, 0x3377d1cf, v10
	v_fmac_f32_e32 v2, 0x3f317217, v10
	v_cmp_lt_f32_e64 vcc, |v10|, s19
	v_lshl_add_u64 v[0:1], s[10:11], 0, v[0:1]
	s_waitcnt vmcnt(2)
	v_fma_f32 v3, -v6, v4, v6
	v_cndmask_b32_e32 v2, v10, v2, vcc
	v_sub_f32_e32 v2, v2, v8
	v_add_f32_e32 v3, v7, v3
	v_add_f32_e32 v2, v2, v3
	s_waitcnt vmcnt(1)
	v_mul_f32_e32 v2, v5, v2
	global_store_dword v[0:1], v2, off
	s_branch .LBB2_8
